# v75 + mLSTM apv/den zero-init moved to the skip path only + 6 self-canonicalising v_max removed from the scan chain + constant grid size in the conversion loop latch
# baseline (speedup 1.0000x reference)
.LBB0_55:
	s_cmp_lg_u32 s99, 0
	s_cbranch_scc1 .Ltc_itemdone
	v_readlane_b32 s2, v254, 0
	v_readlane_b32 s3, v254, 1
	s_movk_i32 s0, 0x100
	s_add_i32 s14, s14, s15
	s_add_i32 s16, s16, s17
	s_add_i32 s10, s10, s18
	s_waitcnt lgkmcnt(0)
	s_add_i32 s22, s22, s0
	s_cmp_lt_i32 s22, 0x13e0
	s_cbranch_scc1 .Ltc_noskip
	s_cmp_ge_i32 s22, 0x2000
	s_cbranch_scc1 .Ltc_noskip
	s_and_b32 s22, s22, 0xff
	s_addk_i32 s22, 0x2000
	s_lshl_b32 s14, s22, 5
	s_lshl_b32 s16, s22, 4
	s_lshl_b32 s10, s22, 9

.LBB0_876:
	s_mov_b32 s46, 0xbfb8aa3b
	s_waitcnt vmcnt(0)
	v_mul_f32_e64 v1, |v213|, s46
	v_exp_f32_e32 v1, v1
	s_mov_b32 s46, 0x800000
	v_max_f32_e32 v2, v213, v213
	v_min_f32_e32 v2, 0, v2
	v_add_f32_e32 v1, 1.0, v1
	v_cmp_gt_f32_e32 vcc, s46, v1
	s_mov_b32 s46, 0x3f317217
	v_lshlrev_b32_e32 v6, 16, v124
	v_cndmask_b32_e64 v3, 0, 32, vcc
	v_ldexp_f32 v1, v1, v3
	v_log_f32_e32 v1, v1
	v_cndmask_b32_e32 v4, 0, v209, vcc
	v_mov_b32_e32 v3, 0
	v_and_b32_e32 v7, 0xffff0000, v124
	v_mul_f32_e32 v5, 0x3f317217, v1
	v_fma_f32 v5, v1, s46, -v5
	v_fmac_f32_e32 v5, 0x3377d1cf, v1
	s_mov_b32 s46, 0x7f800000
	v_fmac_f32_e32 v5, 0x3f317217, v1
	v_cmp_lt_f32_e64 vcc, |v1|, s46
	ds_write_b128 v192, v[116:119]
	ds_write_b128 v192, v[120:123] offset:128
	ds_write_b128 v192, v[124:127] offset:17408
	ds_write_b128 v192, v[128:131] offset:17536
	v_cndmask_b32_e32 v1, v1, v5, vcc
	v_sub_f32_e32 v1, v1, v4
	v_sub_f32_e32 v1, v2, v1
	v_mov_b32_e32 v2, 0
	v_mov_b32_e32 v4, 0xff61b1e6
	v_add_f32_dpp v1, v1, v1 row_shr:1 row_mask:0xf bank_mask:0xf bound_ctrl:1
	v_max_f32_e32 v5, v165, v165
	v_and_b32_e32 v8, 0xffff0000, v125
	v_add_f32_dpp v1, v1, v1 row_shr:2 row_mask:0xf bank_mask:0xf bound_ctrl:1
	v_and_b32_e32 v9, 0xffff0000, v126
	v_and_b32_e32 v10, 0xffff0000, v127
	v_add_f32_dpp v1, v1, v1 row_shr:4 row_mask:0xf bank_mask:0xf bound_ctrl:1
	s_nop 1
	v_add_f32_dpp v1, v1, v1 row_shr:8 row_mask:0xf bank_mask:0xf bound_ctrl:1
	s_nop 1
	v_mov_b32_dpp v3, v1 row_bcast:15 row_mask:0xa bank_mask:0xf
	v_add_f32_e32 v1, v1, v3
	v_mov_b32_e32 v3, 0xff61b1e6
	s_nop 0
	v_mov_b32_dpp v2, v1 row_bcast:31 row_mask:0xc bank_mask:0xf
	v_add_f32_e32 v1, v1, v2
	v_sub_f32_e32 v2, v212, v1
	v_readlane_b32 s70, v1, 63
	s_nop 0
	v_mov_b32_dpp v3, v2 row_shr:1 row_mask:0xf bank_mask:0xf
	v_max_f32_e32 v3, v2, v3
	s_nop 1
	v_mov_b32_dpp v4, v3 row_shr:2 row_mask:0xf bank_mask:0xf
	v_max_f32_e32 v3, v3, v4
	v_mov_b32_e32 v4, 0xff61b1e6
	s_nop 1
	v_mov_b32_dpp v4, v3 row_shr:4 row_mask:0xf bank_mask:0xf
	v_max_f32_e32 v3, v3, v4
	v_mov_b32_e32 v4, 0xff61b1e6
	s_nop 1
	v_mov_b32_dpp v4, v3 row_shr:8 row_mask:0xf bank_mask:0xf
	v_max_f32_e32 v3, v3, v4
	v_mov_b32_e32 v4, 0xff61b1e6
	s_nop 1
	v_mov_b32_dpp v4, v3 row_bcast:15 row_mask:0xa bank_mask:0xf
	v_max_f32_e32 v3, v3, v4
	v_mov_b32_e32 v4, 0xff61b1e6
	s_nop 1
	v_mov_b32_dpp v4, v3 row_bcast:31 row_mask:0xc bank_mask:0xf
	v_max_f32_e32 v4, v3, v4
	s_nop 0
	v_readlane_b32 s46, v4, 63
	s_nop 1
	v_max_f32_e64 v3, s46, s46
	v_max_f32_e32 v3, v5, v3
	v_pk_add_f32 v[14:15], v[2:3], s[70:71] op_sel_hi:[1,0]
	s_nop 0
	v_sub_f32_e32 v3, v14, v15
	v_mul_f32_e32 v3, 0x3fb8aa3b, v3
	v_exp_f32_e32 v3, v3
	s_nop 0
	v_mul_f32_e32 v3, 0x3db504f3, v3
	ds_bpermute_b32 v3, v180, v3
	s_waitcnt lgkmcnt(0)
	v_mul_f32_e32 v6, v6, v3
	v_mul_f32_e32 v7, v7, v3
	v_cvt_pk_bf16_f32 v6, v6, v7
	v_lshlrev_b32_e32 v7, 16, v125
	v_mul_f32_e32 v7, v7, v3
	v_mul_f32_e32 v8, v8, v3
	v_cvt_pk_bf16_f32 v7, v7, v8
	v_lshlrev_b32_e32 v8, 16, v126
	v_mul_f32_e32 v8, v8, v3
	v_mul_f32_e32 v9, v9, v3
	v_cvt_pk_bf16_f32 v8, v8, v9
	v_lshlrev_b32_e32 v9, 16, v127
	v_mul_f32_e32 v9, v9, v3
	v_mul_f32_e32 v10, v10, v3
	v_cvt_pk_bf16_f32 v9, v9, v10
	ds_write_b128 v193, v[6:9] offset:34816
	v_lshlrev_b32_e32 v6, 16, v128
	v_and_b32_e32 v7, 0xffff0000, v128
	v_mul_f32_e32 v6, v6, v3
	v_mul_f32_e32 v7, v7, v3
	v_cvt_pk_bf16_f32 v6, v6, v7
	v_lshlrev_b32_e32 v7, 16, v129
	v_and_b32_e32 v8, 0xffff0000, v129
	v_mul_f32_e32 v7, v7, v3
	v_mul_f32_e32 v8, v8, v3
	v_cvt_pk_bf16_f32 v7, v7, v8
	v_lshlrev_b32_e32 v8, 16, v130
	v_and_b32_e32 v9, 0xffff0000, v130
	v_mul_f32_e32 v8, v8, v3
	v_mul_f32_e32 v9, v9, v3
	v_cvt_pk_bf16_f32 v8, v8, v9
	v_lshlrev_b32_e32 v9, 16, v131
	v_mul_f32_e32 v9, v9, v3
	v_and_b32_e32 v10, 0xffff0000, v131
	v_mul_f32_e32 v3, v10, v3
	v_cvt_pk_bf16_f32 v9, v9, v3
	ds_write_b128 v193, v[6:9] offset:43136
	s_and_saveexec_b64 s[46:47], s[4:5]
	ds_write_b128 v194, v[112:115] offset:51456
	s_or_b64 exec, exec, s[46:47]
	s_andn2_b64 vcc, exec, s[60:61]
	s_cbranch_vccnz .LBB0_880
	v_mul_f32_e32 v2, 0x3fb8aa3b, v2
	ds_write_b32 v182, v2 offset:64832

.LBB0_882:
	ds_read_b128 v[216:219], v196 offset:64320
	ds_read_b128 v[220:223], v196 offset:64336
	ds_read_b128 v[224:227], v196 offset:64384
	ds_read_b128 v[228:231], v196 offset:64400
	s_waitcnt lgkmcnt(10)
	v_mfma_f32_32x32x16_bf16 v[80:95], v[80:83], v[104:107], 0
	v_lshlrev_b32_e32 v108, 16, v104
	v_and_b32_e32 v104, 0xffff0000, v104
	s_waitcnt lgkmcnt(3)
	v_mul_f32_e32 v104, v217, v104
	v_fmac_f32_e32 v104, v216, v108
	v_lshlrev_b32_e32 v108, 16, v105
	v_fmac_f32_e32 v104, v218, v108
	v_and_b32_e32 v105, 0xffff0000, v105
	v_fmac_f32_e32 v104, v219, v105
	v_lshlrev_b32_e32 v105, 16, v106
	s_waitcnt lgkmcnt(2)
	v_fmac_f32_e32 v104, v220, v105
	v_and_b32_e32 v105, 0xffff0000, v106
	v_fmac_f32_e32 v104, v221, v105
	v_lshlrev_b32_e32 v105, 16, v107
	v_fmac_f32_e32 v104, v222, v105
	v_and_b32_e32 v105, 0xffff0000, v107
	v_and_b32_e32 v106, 0xffff0000, v96
	v_fmac_f32_e32 v104, v223, v105
	v_lshlrev_b32_e32 v105, 16, v96
	s_waitcnt lgkmcnt(1)
	v_mul_f32_e32 v106, v225, v106
	v_fmac_f32_e32 v106, v224, v105
	v_lshlrev_b32_e32 v105, 16, v97
	v_fmac_f32_e32 v106, v226, v105
	v_and_b32_e32 v105, 0xffff0000, v97
	v_fmac_f32_e32 v106, v227, v105
	v_lshlrev_b32_e32 v105, 16, v98
	s_waitcnt lgkmcnt(0)
	v_fmac_f32_e32 v106, v228, v105
	v_and_b32_e32 v105, 0xffff0000, v98
	v_fmac_f32_e32 v106, v229, v105
	v_lshlrev_b32_e32 v105, 16, v99
	v_fmac_f32_e32 v106, v230, v105
	v_and_b32_e32 v105, 0xffff0000, v99
	v_mfma_f32_32x32x16_bf16 v[80:95], v[100:103], v[96:99], v[80:95]
	v_add_f32_e32 v104, 0, v104
	v_fmac_f32_e32 v106, v231, v105
	v_add_f32_e32 v167, v104, v106
	ds_bpermute_b32 v214, v189, v167
	s_andn2_b64 vcc, exec, s[62:63]
	s_cbranch_vccnz .Lml_apvz
	v_add_u32_e32 v96, s74, v185
	ds_read_b128 v[216:219], v96 offset:64832
	ds_read_b128 v[220:223], v96 offset:64864
	ds_read_b128 v[224:227], v96 offset:64896
	ds_read_b128 v[228:231], v96 offset:64928
	v_mfma_f32_32x32x16_bf16 v[96:111], v[156:159], v[152:155], 0
	v_fmamk_f32 v215, v215, 0x3fb8aa3b, v197
	s_waitcnt lgkmcnt(3)
	v_sub_f32_e32 v152, v217, v215
	v_exp_f32_e32 v153, v152
	v_sub_f32_e32 v152, v216, v215
	v_sub_f32_e32 v154, v218, v215
	v_sub_f32_e32 v155, v219, v215
	s_waitcnt lgkmcnt(2)
	v_sub_f32_e32 v156, v220, v215
	v_mfma_f32_32x32x16_bf16 v[96:111], v[148:151], v[144:147], v[96:111]
	v_sub_f32_e32 v144, v221, v215
	v_sub_f32_e32 v145, v222, v215
	v_sub_f32_e32 v146, v223, v215
	s_waitcnt lgkmcnt(1)
	v_sub_f32_e32 v147, v224, v215
	v_sub_f32_e32 v157, v225, v215
	v_sub_f32_e32 v158, v226, v215
	v_sub_f32_e32 v159, v227, v215
	v_mfma_f32_32x32x16_bf16 v[96:111], v[140:143], v[136:139], v[96:111]
	s_waitcnt lgkmcnt(0)
	v_sub_f32_e32 v136, v228, v215
	v_sub_f32_e32 v137, v229, v215
	v_sub_f32_e32 v140, v230, v215
	v_sub_f32_e32 v141, v231, v215
	v_exp_f32_e32 v152, v152
	v_exp_f32_e32 v150, v154
	v_exp_f32_e32 v151, v155
	v_mfma_f32_32x32x16_bf16 v[96:111], v[132:135], v[10:13], v[96:111]
	v_exp_f32_e32 v148, v156
	v_exp_f32_e32 v149, v144
	v_exp_f32_e32 v144, v145
	v_exp_f32_e32 v145, v146
	v_exp_f32_e32 v142, v147
	v_exp_f32_e32 v143, v157
	v_exp_f32_e32 v138, v158
	v_exp_f32_e32 v139, v159
	v_exp_f32_e32 v136, v136
	v_exp_f32_e32 v137, v137
	v_exp_f32_e32 v132, v140
	v_exp_f32_e32 v133, v141
	s_andn2_b64 vcc, exec, s[64:65]
	s_mov_b64 s[50:51], -1
	s_cbranch_vccnz .LBB0_885
	v_pk_mul_f32 v[10:11], v[152:153], v[96:97]
	s_mov_b64 s[50:51], 0
	v_add_f32_e32 v12, 0, v10
	v_add_f32_e32 v134, v11, v12
	v_pk_mul_f32 v[12:13], v[150:151], v[98:99]
	s_nop 0
	v_add_f32_e32 v134, v12, v134
	v_add_f32_e32 v140, v13, v134
	v_pk_mul_f32 v[134:135], v[148:149], v[100:101]
	s_nop 0
	v_add_f32_e32 v140, v134, v140
	v_add_f32_e32 v146, v135, v140
	v_pk_mul_f32 v[140:141], v[144:145], v[102:103]
	s_nop 0
	v_add_f32_e32 v146, v140, v146
	v_add_f32_e32 v154, v141, v146
	v_pk_mul_f32 v[146:147], v[142:143], v[104:105]
	s_nop 0
	v_add_f32_e32 v154, v146, v154
	v_add_f32_e32 v156, v147, v154
	v_pk_mul_f32 v[154:155], v[138:139], v[106:107]
	s_nop 0
	v_add_f32_e32 v156, v154, v156
	v_add_f32_e32 v158, v155, v156
	v_pk_mul_f32 v[156:157], v[136:137], v[108:109]
	s_nop 0
	v_add_f32_e32 v158, v156, v158
	v_add_f32_e32 v215, v157, v158
	v_pk_mul_f32 v[158:159], v[132:133], v[110:111]
	s_nop 0
	v_add_f32_e32 v215, v158, v215
	v_add_f32_e32 v215, v159, v215

.Lml_apvz:
	v_mov_b32_e32 v110, 0
	v_mov_b32_e32 v109, 0
	v_mov_b32_e32 v108, 0
	v_mov_b32_e32 v107, 0
	v_mov_b32_e32 v106, 0
	v_mov_b32_e32 v105, 0
	v_mov_b32_e32 v104, 0
	v_mov_b32_e32 v103, 0
	v_mov_b32_e32 v102, 0
	v_mov_b32_e32 v101, 0
	v_mov_b32_e32 v100, 0
	v_mov_b32_e32 v99, 0
	v_mov_b32_e32 v98, 0
	v_mov_b32_e32 v97, 0
	v_mov_b32_e32 v96, 0
	v_mov_b32_e32 v216, 0
	s_branch .LBB0_888
